# speedup vs baseline: 1.0086x; 1.0086x over previous
.LBB1_208:
	s_or_b64 exec, exec, s[0:1]
	v_and_b32_e32 v13, 63, v107
	v_lshrrev_b32_e32 v14, 6, v107
	v_lshlrev_b32_e32 v14, 5, v14
	s_movk_i32 s10, 0xaab
	v_mov_b32_e32 v15, v13
	v_mul_u32_u24_e32 v16, s10, v15
	v_lshrrev_b32_e32 v16, 16, v16
	v_mul_u32_u24_e32 v17, 24, v16
	v_sub_u32_e32 v17, v15, v17
	v_add_u32_e32 v18, v14, v16
	v_lshrrev_b32_e32 v19, 2, v16
	v_lshlrev_b32_e32 v19, 5, v19
	v_lshlrev_b32_e32 v4, 4, v17
	v_xor_b32_e32 v4, v4, v19
	v_mul_u32_u24_e32 v19, 0x180, v18
	v_add_u32_e32 v4, v4, v19
	v_xor_b32_e32 v7, 64, v4
	v_add_u32_e32 v19, v120, v18
	v_mul_u32_u24_e32 v19, 0x300, v19
	v_add_u32_e32 v19, v19, v121
	v_lshl_add_u32 v19, v17, 3, v19
	v_lshlrev_b32_e32 v10, 1, v19
	v_add_u32_e32 v15, 64, v13
	v_mul_u32_u24_e32 v16, s10, v15
	v_lshrrev_b32_e32 v16, 16, v16
	v_mul_u32_u24_e32 v17, 24, v16
	v_sub_u32_e32 v17, v15, v17
	v_add_u32_e32 v18, v14, v16
	v_lshrrev_b32_e32 v19, 2, v16
	v_lshlrev_b32_e32 v19, 5, v19
	v_lshlrev_b32_e32 v5, 4, v17
	v_xor_b32_e32 v5, v5, v19
	v_mul_u32_u24_e32 v19, 0x180, v18
	v_add_u32_e32 v5, v5, v19
	v_xor_b32_e32 v8, 64, v5
	v_add_u32_e32 v19, v120, v18
	v_mul_u32_u24_e32 v19, 0x300, v19
	v_add_u32_e32 v19, v19, v121
	v_lshl_add_u32 v19, v17, 3, v19
	v_lshlrev_b32_e32 v11, 1, v19
	v_add_u32_e32 v15, 128, v13
	v_mul_u32_u24_e32 v16, s10, v15
	v_lshrrev_b32_e32 v16, 16, v16
	v_mul_u32_u24_e32 v17, 24, v16
	v_sub_u32_e32 v17, v15, v17
	v_add_u32_e32 v18, v14, v16
	v_lshrrev_b32_e32 v19, 2, v16
	v_lshlrev_b32_e32 v19, 5, v19
	v_lshlrev_b32_e32 v6, 4, v17
	v_xor_b32_e32 v6, v6, v19
	v_mul_u32_u24_e32 v19, 0x180, v18
	v_add_u32_e32 v6, v6, v19
	v_xor_b32_e32 v9, 64, v6
	v_add_u32_e32 v19, v120, v18
	v_mul_u32_u24_e32 v19, 0x300, v19
	v_add_u32_e32 v19, v19, v121
	v_lshl_add_u32 v19, v17, 3, v19
	v_lshlrev_b32_e32 v12, 1, v19
	s_waitcnt lgkmcnt(0)
	s_barrier
	s_waitcnt vmcnt(0)
	s_and_saveexec_b64 s[100:101], s[34:35]
	s_cbranch_execz .Lpf_skip_g1
	v_readfirstlane_b32 s10, v173
	s_lshl_b32 s10, s10, 7
	s_add_u32 s10, s64, s10
	s_addc_u32 s11, s65, 0
	global_atomic_add v231, v109, v1, s[10:11] sc0

.Lpf_end_g1:
	ds_read_b128 v[20:23], v4
	ds_read_b128 v[24:27], v5
	ds_read_b128 v[28:31], v6
	ds_read_b128 v[32:35], v7 offset:3072
	ds_read_b128 v[36:39], v8 offset:3072
	ds_read_b128 v[40:43], v9 offset:3072
	ds_read_b128 v[44:47], v4 offset:6144
	ds_read_b128 v[48:51], v5 offset:6144
	ds_read_b128 v[52:55], v6 offset:6144
	ds_read_b128 v[56:59], v7 offset:9216
	ds_read_b128 v[60:63], v8 offset:9216
	ds_read_b128 v[64:67], v9 offset:9216
	v_cmp_eq_u32_e32 vcc, 0, v107
	s_waitcnt lgkmcnt(11)
	global_store_dwordx4 v10, v[20:23], s[44:45]
	s_waitcnt lgkmcnt(10)
	global_store_dwordx4 v11, v[24:27], s[44:45]
	s_waitcnt lgkmcnt(9)
	global_store_dwordx4 v12, v[28:31], s[44:45]
	v_add_u32_e32 v16, 0x3000, v10
	s_waitcnt lgkmcnt(8)
	global_store_dwordx4 v16, v[32:35], s[44:45]
	v_add_u32_e32 v16, 0x3000, v11
	s_waitcnt lgkmcnt(7)
	global_store_dwordx4 v16, v[36:39], s[44:45]
	v_add_u32_e32 v16, 0x3000, v12
	s_waitcnt lgkmcnt(6)
	global_store_dwordx4 v16, v[40:43], s[44:45]
	v_add_u32_e32 v16, 0x6000, v10
	s_waitcnt lgkmcnt(5)
	global_store_dwordx4 v16, v[44:47], s[44:45]
	v_add_u32_e32 v16, 0x6000, v11
	s_waitcnt lgkmcnt(4)
	global_store_dwordx4 v16, v[48:51], s[44:45]
	v_add_u32_e32 v16, 0x6000, v12
	s_waitcnt lgkmcnt(3)
	global_store_dwordx4 v16, v[52:55], s[44:45]
	v_add_u32_e32 v16, 0x9000, v10
	s_waitcnt lgkmcnt(2)
	global_store_dwordx4 v16, v[56:59], s[44:45]
	v_add_u32_e32 v16, 0x9000, v11
	s_waitcnt lgkmcnt(1)
	global_store_dwordx4 v16, v[60:63], s[44:45]
	v_add_u32_e32 v16, 0x9000, v12
	s_waitcnt lgkmcnt(0)
	global_store_dwordx4 v16, v[64:67], s[44:45]
	s_waitcnt vmcnt(0)
	s_barrier
	s_and_saveexec_b64 s[0:1], vcc
	s_cbranch_execz .LBB1_210
	v_lshl_add_u64 v[2:3], v[98:99], 2, s[96:97]
	s_waitcnt vmcnt(0)
	global_atomic_add v[2:3], v1, off
